# GEMM accumulators zeroed by 32 two-pass 4x4x1 f32 MFMAs per unit instead of 128 v_mov; split-counter posts save/restore exec
# speedup vs baseline: 1.0025x; 1.0025x over previous
.LBB0_219:
	s_ashr_i32 s47, s46, 31
	s_lshl_b64 s[50:51], s[46:47], 19
	s_add_u32 s50, s64, s50
	s_addc_u32 s51, s65, s51
	s_and_b64 s[52:53], s[48:49], exec
	s_cselect_b32 s9, s51, s57
	s_cselect_b32 s47, s50, s56
	s_ashr_i32 s45, s44, 31
	s_lshl_b64 s[52:53], s[44:45], 19
	s_add_u32 s52, s66, s52
	s_addc_u32 s53, s67, s53
	s_and_b64 s[60:61], s[48:49], exec
	s_cselect_b32 s45, s53, s59
	s_cselect_b32 s55, s52, s58
	s_add_u32 s56, s56, 0x80
	s_addc_u32 s57, s57, 0
	s_add_u32 s80, s58, 0x100
	v_mov_b32_e32 v0, 0
	s_addc_u32 s81, s59, 0
	s_mov_b32 s82, -2
	s_nop 1
	v_mfma_f32_4x4x1_16b_f32 v[4:7], v0, v0, 0
	v_mfma_f32_4x4x1_16b_f32 v[8:11], v0, v0, 0
	v_mfma_f32_4x4x1_16b_f32 v[12:15], v0, v0, 0
	v_mfma_f32_4x4x1_16b_f32 v[16:19], v0, v0, 0
	v_mfma_f32_4x4x1_16b_f32 v[20:23], v0, v0, 0
	v_mfma_f32_4x4x1_16b_f32 v[24:27], v0, v0, 0
	v_mfma_f32_4x4x1_16b_f32 v[28:31], v0, v0, 0
	v_mfma_f32_4x4x1_16b_f32 v[32:35], v0, v0, 0
	v_mfma_f32_4x4x1_16b_f32 v[36:39], v0, v0, 0
	v_mfma_f32_4x4x1_16b_f32 v[40:43], v0, v0, 0
	v_mfma_f32_4x4x1_16b_f32 v[44:47], v0, v0, 0
	v_mfma_f32_4x4x1_16b_f32 v[48:51], v0, v0, 0
	v_mfma_f32_4x4x1_16b_f32 v[52:55], v0, v0, 0
	v_mfma_f32_4x4x1_16b_f32 v[56:59], v0, v0, 0
	v_mfma_f32_4x4x1_16b_f32 v[60:63], v0, v0, 0
	v_mfma_f32_4x4x1_16b_f32 v[64:67], v0, v0, 0
	v_mfma_f32_4x4x1_16b_f32 v[68:71], v0, v0, 0
	v_mfma_f32_4x4x1_16b_f32 v[72:75], v0, v0, 0
	v_mfma_f32_4x4x1_16b_f32 v[76:79], v0, v0, 0
	v_mfma_f32_4x4x1_16b_f32 v[80:83], v0, v0, 0
	v_mfma_f32_4x4x1_16b_f32 v[84:87], v0, v0, 0
	v_mfma_f32_4x4x1_16b_f32 v[88:91], v0, v0, 0
	v_mfma_f32_4x4x1_16b_f32 v[92:95], v0, v0, 0
	v_mfma_f32_4x4x1_16b_f32 v[96:99], v0, v0, 0
	v_mfma_f32_4x4x1_16b_f32 v[100:103], v0, v0, 0
	v_mfma_f32_4x4x1_16b_f32 v[104:107], v0, v0, 0
	v_mfma_f32_4x4x1_16b_f32 v[108:111], v0, v0, 0
	v_mfma_f32_4x4x1_16b_f32 v[112:115], v0, v0, 0
	v_mfma_f32_4x4x1_16b_f32 v[116:119], v0, v0, 0
	v_mfma_f32_4x4x1_16b_f32 v[120:123], v0, v0, 0
	v_mfma_f32_4x4x1_16b_f32 v[124:127], v0, v0, 0
	v_mfma_f32_4x4x1_16b_f32 v[0:3], v0, v0, 0

.LBB0_370:
	s_bfe_u32 s9, s8, 0x10005
	s_lshl_b32 s2, s8, 1
	s_and_b32 s10, s2, 62
	s_lshl_b32 s2, s9, 13
	s_ashr_i32 s0, s8, 6
	s_or_b32 s11, s2, s10
	s_lshl_b32 s2, s0, 7
	v_add_u32_e32 v2, s11, v41
	v_add_u32_e32 v4, s11, v42
	s_ashr_i32 s3, s2, 31
	v_ashrrev_i32_e32 v3, 31, v2
	v_ashrrev_i32_e32 v5, 31, v4
	v_lshl_add_u64 v[0:1], s[2:3], 1, v[32:33]
	v_lshlrev_b64 v[2:3], 10, v[2:3]
	v_lshlrev_b64 v[4:5], 10, v[4:5]
	v_lshl_add_u64 v[2:3], v[0:1], 0, v[2:3]
	v_lshl_add_u64 v[4:5], v[0:1], 0, v[4:5]
	global_load_dwordx4 v[60:63], v[2:3], off
	global_load_dwordx4 v[64:67], v[4:5], off
	v_add_u32_e32 v2, s11, v43
	v_add_u32_e32 v4, s11, v44
	v_ashrrev_i32_e32 v3, 31, v2
	v_ashrrev_i32_e32 v5, 31, v4
	v_lshlrev_b64 v[2:3], 10, v[2:3]
	v_lshlrev_b64 v[4:5], 10, v[4:5]
	v_lshl_add_u64 v[2:3], v[0:1], 0, v[2:3]
	v_lshl_add_u64 v[4:5], v[0:1], 0, v[4:5]
	global_load_dwordx4 v[68:71], v[2:3], off
	global_load_dwordx4 v[72:75], v[4:5], off
	v_add_u32_e32 v2, s11, v45
	v_add_u32_e32 v4, s11, v46
	v_ashrrev_i32_e32 v3, 31, v2
	v_ashrrev_i32_e32 v5, 31, v4
	v_lshlrev_b64 v[2:3], 10, v[2:3]
	v_lshlrev_b64 v[4:5], 10, v[4:5]
	v_lshl_add_u64 v[2:3], v[0:1], 0, v[2:3]
	v_lshl_add_u64 v[4:5], v[0:1], 0, v[4:5]
	global_load_dwordx4 v[76:79], v[2:3], off
	global_load_dwordx4 v[80:83], v[4:5], off
	v_add_u32_e32 v2, s11, v47
	v_add_u32_e32 v4, s11, v48
	v_ashrrev_i32_e32 v3, 31, v2
	v_ashrrev_i32_e32 v5, 31, v4
	v_lshlrev_b64 v[2:3], 10, v[2:3]
	v_lshlrev_b64 v[4:5], 10, v[4:5]
	v_lshl_add_u64 v[2:3], v[0:1], 0, v[2:3]
	v_lshl_add_u64 v[0:1], v[0:1], 0, v[4:5]
	s_lshl_b32 s0, s0, 8
	global_load_dwordx4 v[84:87], v[2:3], off
	global_load_dwordx4 v[88:91], v[0:1], off
	v_add_u32_e32 v0, s0, v38
	v_ashrrev_i32_e32 v1, 31, v0
	v_lshlrev_b64 v[0:1], 8, v[0:1]
	v_lshl_add_u64 v[58:59], v[34:35], 0, v[0:1]
	v_add_u32_e32 v0, s0, v39
	v_ashrrev_i32_e32 v1, 31, v0
	v_lshlrev_b64 v[0:1], 8, v[0:1]
	v_lshl_add_u64 v[92:93], v[34:35], 0, v[0:1]
	global_load_dwordx4 v[0:3], v[58:59], off
	global_load_dwordx4 v[4:7], v[58:59], off offset:64
	global_load_dwordx4 v[8:11], v[92:93], off
	global_load_dwordx4 v[12:15], v[92:93], off offset:64
	global_load_dwordx4 v[16:19], v[58:59], off offset:128
	global_load_dwordx4 v[20:23], v[58:59], off offset:192
	global_load_dwordx4 v[24:27], v[92:93], off offset:128
	global_load_dwordx4 v[28:31], v[92:93], off offset:192
	s_lshl_b32 s0, s9, 6
	s_mov_b32 s3, s1
	v_mov_b32_e32 v58, v49
	s_or_b32 s9, s0, s10
	v_add_u32_e32 v59, s2, v40
	s_mov_b32 s2, s1
	s_waitcnt vmcnt(16)
	s_barrier
	s_cmp_lg_u32 s99, 0
	s_cbranch_scc1 .Lsc1_post_skip
	v_readlane_b32 s99, v235, 9
	v_readlane_b32 s100, v235, 7
	v_readlane_b32 s101, v235, 8
	s_lshl_b32 s99, s99, 8
	s_addk_i32 s99, 0x1c00
	s_add_u32 s100, s100, s99
	s_addc_u32 s101, s101, 0
	v_mov_b32_e32 v240, s100
	v_mov_b32_e32 v241, s101
	v_mov_b32_e32 v237, 1
	s_mov_b64 s[100:101], exec
	s_mov_b64 exec, 1
	s_nop 1
	global_atomic_add v238, v[240:241], v237, off sc0
	s_mov_b64 exec, s[100:101]
	s_mov_b32 s99, 1
.Lsc1_post_skip:
	s_waitcnt vmcnt(15)
	ds_write_b128 v50, v[60:63]
	s_waitcnt vmcnt(14)
	ds_write_b128 v51, v[64:67]
	s_waitcnt vmcnt(13)
	ds_write_b128 v52, v[68:71]
	s_waitcnt vmcnt(12)
	ds_write_b128 v53, v[72:75]
	s_waitcnt vmcnt(11)
	ds_write_b128 v54, v[76:79]
	s_waitcnt vmcnt(10)
	ds_write_b128 v55, v[80:83]
	s_waitcnt vmcnt(9)
	ds_write_b128 v56, v[84:87]
	s_waitcnt vmcnt(8)
	ds_write_b128 v57, v[88:91]
	s_waitcnt lgkmcnt(0)
	s_barrier
	s_waitcnt vmcnt(0)
	s_cmp_lg_u32 s99, 1
	s_cbranch_scc1 .Lsc1_chk_skip
	s_mov_b32 s99, 2
	v_mov_b32_e32 v239, 0x20000
	ds_read_b32 v239, v239
	v_add_u32_e32 v238, 1, v238
	s_waitcnt lgkmcnt(0)
	v_readfirstlane_b32 s100, v238
	v_readfirstlane_b32 s101, v239
	s_nop 0
	s_cmp_lg_u32 s100, s101
	s_cbranch_scc1 .Lsc1_chk_skip
	buffer_wbl2 sc1
	s_waitcnt vmcnt(0)
	v_readlane_b32 s100, v235, 7
	v_readlane_b32 s101, v235, 8
	s_nop 0
	s_add_u32 s100, s100, 0x2c00
	s_addc_u32 s101, s101, 0
	v_mov_b32_e32 v240, s100
	v_mov_b32_e32 v241, s101
	v_mov_b32_e32 v237, 1
	s_mov_b64 s[100:101], exec
	s_mov_b64 exec, 1
	s_nop 1
	global_atomic_add v[240:241], v237, off
	s_mov_b64 exec, s[100:101]

.LBB0_497:
	v_add_u32_e32 v18, s26, v162
	v_add_u32_e32 v16, 64, v18
	v_add_u32_e32 v18, 0x60, v18
	v_ashrrev_i32_e32 v17, 31, v16
	v_ashrrev_i32_e32 v19, 31, v18
	v_lshlrev_b64 v[16:17], 11, v[16:17]
	v_lshlrev_b64 v[18:19], 11, v[18:19]
	v_lshl_add_u64 v[16:17], v[136:137], 0, v[16:17]
	v_lshl_add_u64 v[18:19], v[136:137], 0, v[18:19]
	v_add_u32_e32 v138, s26, v133
	ds_write_b128 v159, v[52:55]
	ds_write_b128 v159, v[64:67] offset:8704
	ds_write_b128 v159, v[56:59] offset:17408
	ds_write_b128 v159, v[60:63] offset:26112
	s_waitcnt lgkmcnt(0)
	s_barrier
	s_cmp_lg_u32 s99, 0
	s_cbranch_scc1 .Lsc2_post_skip
	v_readlane_b32 s99, v235, 9
	v_readlane_b32 s100, v235, 7
	v_readlane_b32 s101, v235, 8
	s_lshl_b32 s99, s99, 8
	s_addk_i32 s99, 0x1c80
	s_add_u32 s100, s100, s99
	s_addc_u32 s101, s101, 0
	v_mov_b32_e32 v240, s100
	v_mov_b32_e32 v241, s101
	v_mov_b32_e32 v237, 1
	s_mov_b64 s[100:101], exec
	s_mov_b64 exec, 1
	s_nop 1
	global_atomic_add v238, v[240:241], v237, off sc0
	s_mov_b64 exec, s[100:101]
	s_mov_b32 s99, 1
.Lsc2_post_skip:
	global_load_dwordx4 v[52:55], v[16:17], off nt
	global_load_dwordx4 v[64:67], v[18:19], off nt
	global_load_dwordx4 v[56:59], v[16:17], off offset:1024 nt
	global_load_dwordx4 v[60:63], v[18:19], off offset:1024 nt
	v_add_u32_e32 v16, 64, v138
	v_ashrrev_i32_e32 v17, 31, v16
	v_lshlrev_b64 v[16:17], 10, v[16:17]
	v_lshl_or_b32 v16, v134, 1, v16
	v_lshl_add_u64 v[18:19], s[8:9], 0, v[16:17]
	global_load_dwordx4 v[40:43], v[18:19], off offset:16 nt
	global_load_dwordx4 v[24:27], v[18:19], off nt
	v_lshl_add_u64 v[18:19], s[10:11], 0, v[16:17]
	v_lshl_add_u64 v[16:17], s[6:7], 0, v[16:17]
	global_load_dwordx4 v[32:35], v[18:19], off offset:16 nt
	global_load_dwordx4 v[20:23], v[18:19], off nt
	global_load_dwordx4 v[36:39], v[16:17], off offset:16 nt
	s_nop 0
	global_load_dwordx4 v[16:19], v[16:17], off nt
	ds_read2_b64 v[112:115], v156 offset1:4
	ds_read2_b64 v[148:151], v156 offset0:8 offset1:12
	v_add_u32_e32 v163, 0x1000, v156
	s_waitcnt lgkmcnt(1)
	v_mfma_f32_16x16x32_bf16 v[112:115], v[112:115], v[84:87], 0
	ds_read2_b64 v[116:119], v163 offset0:32 offset1:36
	v_add_u32_e32 v164, 0x2000, v156
	ds_read2_b64 v[140:143], v164 offset0:64 offset1:68
	s_waitcnt lgkmcnt(2)
	v_mfma_f32_16x16x32_bf16 v[112:115], v[148:151], v[80:83], v[112:115]
	ds_read2_b64 v[148:151], v163 offset0:40 offset1:44
	v_add_u32_e32 v165, 0x3000, v156
	ds_read2_b64 v[144:147], v165 offset0:96 offset1:100
	s_waitcnt lgkmcnt(3)
	v_mfma_f32_16x16x32_bf16 v[116:119], v[116:119], v[84:87], 0
	v_add_u32_e32 v166, 0x4000, v156
	v_add_u32_e32 v167, 0x5000, v156
	v_add_u32_e32 v168, 0x6000, v156
	s_waitcnt lgkmcnt(1)
	v_mfma_f32_16x16x32_bf16 v[116:119], v[148:151], v[80:83], v[116:119]
	ds_read2_b64 v[148:151], v164 offset0:72 offset1:76
	v_add_u32_e32 v169, 0x7000, v156
	v_add_u32_e32 v170, 0x8800, v160
	v_mfma_f32_16x16x32_bf16 v[140:143], v[140:143], v[84:87], 0
	v_add_u32_e32 v171, 0x8c00, v160
	v_add_u32_e32 v172, 0xa800, v160
	v_add_u32_e32 v173, 0xac00, v160
	s_waitcnt lgkmcnt(0)
	v_mfma_f32_16x16x32_bf16 v[140:143], v[148:151], v[80:83], v[140:143]
	ds_read2_b64 v[148:151], v165 offset0:104 offset1:108
	v_add_u32_e32 v174, 0xca00, v160
	v_add_u32_e32 v175, 0xce00, v160
	v_mfma_f32_16x16x32_bf16 v[144:147], v[144:147], v[84:87], 0
	v_add_u32_e32 v176, 0xea00, v160
	v_add_u32_e32 v177, 0xee00, v160
	v_ashrrev_i32_e32 v139, 31, v138
	s_waitcnt lgkmcnt(0)
	v_mfma_f32_16x16x32_bf16 v[144:147], v[148:151], v[80:83], v[144:147]
	ds_read2_b64 v[148:151], v156 offset0:16 offset1:20
	v_lshlrev_b32_e32 v122, 1, v120
	s_add_i32 s26, s26, 64
	s_waitcnt lgkmcnt(0)
	v_mfma_f32_16x16x32_bf16 v[112:115], v[148:151], v[76:79], v[112:115]
	ds_read2_b64 v[148:151], v163 offset0:48 offset1:52
	s_cmpk_eq_i32 s26, 0xc0
	s_waitcnt lgkmcnt(0)
	v_mfma_f32_16x16x32_bf16 v[116:119], v[148:151], v[76:79], v[116:119]
	ds_read2_b64 v[148:151], v164 offset0:80 offset1:84
	s_waitcnt lgkmcnt(0)
	v_mfma_f32_16x16x32_bf16 v[140:143], v[148:151], v[76:79], v[140:143]
	ds_read2_b64 v[148:151], v165 offset0:112 offset1:116
	s_waitcnt lgkmcnt(0)
	v_mfma_f32_16x16x32_bf16 v[144:147], v[148:151], v[76:79], v[144:147]
	ds_read2_b64 v[148:151], v156 offset0:24 offset1:28
	s_waitcnt lgkmcnt(0)
	v_mfma_f32_16x16x32_bf16 v[112:115], v[148:151], v[72:75], v[112:115]
	ds_read2_b64 v[148:151], v163 offset0:56 offset1:60
	s_waitcnt lgkmcnt(0)
	v_mfma_f32_16x16x32_bf16 v[116:119], v[148:151], v[72:75], v[116:119]
	ds_read2_b64 v[148:151], v164 offset0:88 offset1:92
	s_waitcnt lgkmcnt(0)
	v_mfma_f32_16x16x32_bf16 v[140:143], v[148:151], v[72:75], v[140:143]
	ds_read2_b64 v[148:151], v165 offset0:120 offset1:124
	s_waitcnt lgkmcnt(0)
	v_mfma_f32_16x16x32_bf16 v[144:147], v[148:151], v[72:75], v[144:147]
	ds_read2_b64 v[148:151], v166 offset0:128 offset1:132
	s_waitcnt lgkmcnt(0)
	v_mfma_f32_16x16x32_bf16 v[112:115], v[148:151], v[68:71], v[112:115]
	ds_read2_b64 v[148:151], v167 offset0:160 offset1:164
	s_waitcnt lgkmcnt(0)
	v_mfma_f32_16x16x32_bf16 v[116:119], v[148:151], v[68:71], v[116:119]
	ds_read2_b64 v[148:151], v168 offset0:192 offset1:196
	s_waitcnt lgkmcnt(0)
	v_mfma_f32_16x16x32_bf16 v[140:143], v[148:151], v[68:71], v[140:143]
	ds_read2_b64 v[148:151], v169 offset0:224 offset1:228
	s_waitcnt lgkmcnt(0)
	v_mfma_f32_16x16x32_bf16 v[144:147], v[148:151], v[68:71], v[144:147]
	ds_read2_b64 v[148:151], v166 offset0:136 offset1:140
	s_waitcnt lgkmcnt(0)
	v_mfma_f32_16x16x32_bf16 v[112:115], v[148:151], v[48:51], v[112:115]
	ds_read2_b64 v[148:151], v167 offset0:168 offset1:172
	s_waitcnt lgkmcnt(0)
	v_mfma_f32_16x16x32_bf16 v[116:119], v[148:151], v[48:51], v[116:119]
	ds_read2_b64 v[148:151], v168 offset0:200 offset1:204
	s_waitcnt lgkmcnt(0)
	v_mfma_f32_16x16x32_bf16 v[140:143], v[148:151], v[48:51], v[140:143]
	ds_read2_b64 v[148:151], v169 offset0:232 offset1:236
	s_waitcnt lgkmcnt(0)
	v_mfma_f32_16x16x32_bf16 v[144:147], v[148:151], v[48:51], v[144:147]
	ds_read2_b64 v[148:151], v166 offset0:144 offset1:148
	s_waitcnt lgkmcnt(0)
	v_mfma_f32_16x16x32_bf16 v[112:115], v[148:151], v[44:47], v[112:115]
	ds_read2_b64 v[148:151], v167 offset0:176 offset1:180
	s_waitcnt lgkmcnt(0)
	v_mfma_f32_16x16x32_bf16 v[116:119], v[148:151], v[44:47], v[116:119]
	ds_read2_b64 v[148:151], v168 offset0:208 offset1:212
	s_waitcnt lgkmcnt(0)
	v_mfma_f32_16x16x32_bf16 v[140:143], v[148:151], v[44:47], v[140:143]
	ds_read2_b64 v[148:151], v169 offset0:240 offset1:244
	s_waitcnt lgkmcnt(0)
	v_mfma_f32_16x16x32_bf16 v[144:147], v[148:151], v[44:47], v[144:147]
	ds_read2_b64 v[148:151], v166 offset0:152 offset1:156
	s_waitcnt lgkmcnt(0)
	v_mfma_f32_16x16x32_bf16 v[112:115], v[148:151], v[28:31], v[112:115]
	ds_read2_b64 v[148:151], v167 offset0:184 offset1:188
	s_waitcnt lgkmcnt(0)
	v_mfma_f32_16x16x32_bf16 v[116:119], v[148:151], v[28:31], v[116:119]
	ds_read2_b64 v[148:151], v168 offset0:216 offset1:220
	s_waitcnt lgkmcnt(0)
	v_mfma_f32_16x16x32_bf16 v[140:143], v[148:151], v[28:31], v[140:143]
	ds_read2_b64 v[148:151], v169 offset0:248 offset1:252
	s_nop 0
	ds_write2_b32 v170, v112, v113 offset1:132
	ds_write2_b32 v171, v114, v115 offset0:8 offset1:140
	s_waitcnt lgkmcnt(2)
	v_mfma_f32_16x16x32_bf16 v[144:147], v[148:151], v[28:31], v[144:147]
	ds_write2_b32 v172, v116, v117 offset0:64 offset1:196
	ds_write2_b32 v173, v118, v119 offset0:72 offset1:204
	ds_write2_b32 v174, v140, v141 offset1:132
	ds_write2_b32 v175, v142, v143 offset0:8 offset1:140
	s_nop 3
	ds_write2_b32 v176, v144, v145 offset0:64 offset1:196
	ds_write2_b32 v177, v146, v147 offset0:72 offset1:204
	s_waitcnt lgkmcnt(0)
	s_barrier
	s_cmp_lg_u32 s99, 1
	s_cbranch_scc1 .Lsc2_chk_skip
	s_mov_b32 s99, 2
	s_waitcnt vmcnt(10)
	v_mov_b32_e32 v239, 0x20000
	ds_read_b32 v239, v239
	v_add_u32_e32 v238, 1, v238
	s_waitcnt lgkmcnt(0)
	v_readfirstlane_b32 s100, v238
	v_readfirstlane_b32 s101, v239
	s_nop 0
	s_cmp_lg_u32 s100, s101
	s_cbranch_scc1 .Lsc2_chk_skip
	buffer_wbl2 sc1
	s_waitcnt vmcnt(0)
	v_readlane_b32 s100, v235, 7
	v_readlane_b32 s101, v235, 8
	s_nop 0
	s_add_u32 s100, s100, 0x2c80
	s_addc_u32 s101, s101, 0
	v_mov_b32_e32 v240, s100
	v_mov_b32_e32 v241, s101
	v_mov_b32_e32 v237, 1
	s_mov_b64 s[100:101], exec
	s_mov_b64 exec, 1
	s_nop 1
	global_atomic_add v[240:241], v237, off
	s_mov_b64 exec, s[100:101]

.LBB0_565:
	s_ashr_i32 s21, s20, 31
	s_lshl_b64 s[28:29], s[20:21], 19
	s_add_u32 s28, s33, s28
	s_addc_u32 s29, s42, s29
	s_and_b64 s[30:31], s[26:27], exec
	s_cselect_b32 s21, s29, s37
	s_cselect_b32 s56, s28, s36
	s_ashr_i32 s23, s22, 31
	s_lshl_b64 s[30:31], s[22:23], 19
	s_add_u32 s30, s43, s30
	s_addc_u32 s31, s44, s31
	s_and_b64 s[40:41], s[26:27], exec
	s_cselect_b32 s23, s31, s39
	s_cselect_b32 s57, s30, s38
	s_add_u32 s36, s36, 0x80
	s_addc_u32 s37, s37, 0
	s_add_u32 s58, s38, 0x100
	v_mov_b32_e32 v0, 0
	s_addc_u32 s59, s39, 0
	s_mov_b32 s60, -2
	s_nop 1
	v_mfma_f32_4x4x1_16b_f32 v[4:7], v0, v0, 0
	v_mfma_f32_4x4x1_16b_f32 v[8:11], v0, v0, 0
	v_mfma_f32_4x4x1_16b_f32 v[12:15], v0, v0, 0
	v_mfma_f32_4x4x1_16b_f32 v[16:19], v0, v0, 0
	v_mfma_f32_4x4x1_16b_f32 v[20:23], v0, v0, 0
	v_mfma_f32_4x4x1_16b_f32 v[24:27], v0, v0, 0
	v_mfma_f32_4x4x1_16b_f32 v[28:31], v0, v0, 0
	v_mfma_f32_4x4x1_16b_f32 v[32:35], v0, v0, 0
	v_mfma_f32_4x4x1_16b_f32 v[36:39], v0, v0, 0
	v_mfma_f32_4x4x1_16b_f32 v[40:43], v0, v0, 0
	v_mfma_f32_4x4x1_16b_f32 v[44:47], v0, v0, 0
	v_mfma_f32_4x4x1_16b_f32 v[48:51], v0, v0, 0
	v_mfma_f32_4x4x1_16b_f32 v[52:55], v0, v0, 0
	v_mfma_f32_4x4x1_16b_f32 v[56:59], v0, v0, 0
	v_mfma_f32_4x4x1_16b_f32 v[60:63], v0, v0, 0
	v_mfma_f32_4x4x1_16b_f32 v[64:67], v0, v0, 0
	v_mfma_f32_4x4x1_16b_f32 v[68:71], v0, v0, 0
	v_mfma_f32_4x4x1_16b_f32 v[72:75], v0, v0, 0
	v_mfma_f32_4x4x1_16b_f32 v[76:79], v0, v0, 0
	v_mfma_f32_4x4x1_16b_f32 v[80:83], v0, v0, 0
	v_mfma_f32_4x4x1_16b_f32 v[84:87], v0, v0, 0
	v_mfma_f32_4x4x1_16b_f32 v[88:91], v0, v0, 0
	v_mfma_f32_4x4x1_16b_f32 v[92:95], v0, v0, 0
	v_mfma_f32_4x4x1_16b_f32 v[96:99], v0, v0, 0
	v_mfma_f32_4x4x1_16b_f32 v[100:103], v0, v0, 0
	v_mfma_f32_4x4x1_16b_f32 v[104:107], v0, v0, 0
	v_mfma_f32_4x4x1_16b_f32 v[108:111], v0, v0, 0
	v_mfma_f32_4x4x1_16b_f32 v[112:115], v0, v0, 0
	v_mfma_f32_4x4x1_16b_f32 v[116:119], v0, v0, 0
	v_mfma_f32_4x4x1_16b_f32 v[120:123], v0, v0, 0
	v_mfma_f32_4x4x1_16b_f32 v[124:127], v0, v0, 0
	v_mfma_f32_4x4x1_16b_f32 v[0:3], v0, v0, 0
	s_waitcnt vmcnt(0)

.LBB0_1039:
	s_ashr_i32 s15, s14, 31
	s_lshl_b64 s[18:19], s[14:15], 18
	s_add_u32 s18, s9, s18
	s_addc_u32 s19, s11, s19
	s_and_b64 s[20:21], s[16:17], exec
	s_cselect_b32 s15, s19, s35
	s_cselect_b32 s55, s18, s34
	s_ashr_i32 s13, s12, 31
	s_lshl_b64 s[20:21], s[12:13], 18
	s_add_u32 s20, s23, s20
	s_addc_u32 s21, s40, s21
	s_and_b64 s[38:39], s[16:17], exec
	s_cselect_b32 s13, s21, s37
	s_cselect_b32 s56, s20, s36
	s_add_u32 s34, s34, 0x80
	s_addc_u32 s35, s35, 0
	s_add_u32 s57, s36, 0x100
	v_mov_b32_e32 v32, 0
	s_addc_u32 s58, s37, 0
	s_mov_b32 s59, -2
	s_nop 1
	v_mfma_f32_4x4x1_16b_f32 v[36:39], v32, v32, 0
	v_mfma_f32_4x4x1_16b_f32 v[40:43], v32, v32, 0
	v_mfma_f32_4x4x1_16b_f32 v[44:47], v32, v32, 0
	v_mfma_f32_4x4x1_16b_f32 v[48:51], v32, v32, 0
	v_mfma_f32_4x4x1_16b_f32 v[52:55], v32, v32, 0
	v_mfma_f32_4x4x1_16b_f32 v[56:59], v32, v32, 0
	v_mfma_f32_4x4x1_16b_f32 v[60:63], v32, v32, 0
	v_mfma_f32_4x4x1_16b_f32 v[64:67], v32, v32, 0
	v_mfma_f32_4x4x1_16b_f32 v[68:71], v32, v32, 0
	v_mfma_f32_4x4x1_16b_f32 v[72:75], v32, v32, 0
	v_mfma_f32_4x4x1_16b_f32 v[76:79], v32, v32, 0
	v_mfma_f32_4x4x1_16b_f32 v[80:83], v32, v32, 0
	v_mfma_f32_4x4x1_16b_f32 v[84:87], v32, v32, 0
	v_mfma_f32_4x4x1_16b_f32 v[88:91], v32, v32, 0
	v_mfma_f32_4x4x1_16b_f32 v[92:95], v32, v32, 0
	v_mfma_f32_4x4x1_16b_f32 v[96:99], v32, v32, 0
	v_mfma_f32_4x4x1_16b_f32 v[100:103], v32, v32, 0
	v_mfma_f32_4x4x1_16b_f32 v[104:107], v32, v32, 0
	v_mfma_f32_4x4x1_16b_f32 v[108:111], v32, v32, 0
	v_mfma_f32_4x4x1_16b_f32 v[112:115], v32, v32, 0
	v_mfma_f32_4x4x1_16b_f32 v[116:119], v32, v32, 0
	v_mfma_f32_4x4x1_16b_f32 v[120:123], v32, v32, 0
	v_mfma_f32_4x4x1_16b_f32 v[124:127], v32, v32, 0
	v_mfma_f32_4x4x1_16b_f32 v[128:131], v32, v32, 0
	v_mfma_f32_4x4x1_16b_f32 v[132:135], v32, v32, 0
	v_mfma_f32_4x4x1_16b_f32 v[136:139], v32, v32, 0
	v_mfma_f32_4x4x1_16b_f32 v[140:143], v32, v32, 0
	v_mfma_f32_4x4x1_16b_f32 v[144:147], v32, v32, 0
	v_mfma_f32_4x4x1_16b_f32 v[148:151], v32, v32, 0
	v_mfma_f32_4x4x1_16b_f32 v[152:155], v32, v32, 0
	v_mfma_f32_4x4x1_16b_f32 v[156:159], v32, v32, 0
	v_mfma_f32_4x4x1_16b_f32 v[32:35], v32, v32, 0

.LBB0_1180:
	s_add_u32 s60, s0, 0x100
	v_mov_b32_e32 v32, 0
	s_addc_u32 s61, s1, 0
	s_mov_b32 s62, -2
	s_nop 1
	v_mfma_f32_4x4x1_16b_f32 v[36:39], v32, v32, 0
	v_mfma_f32_4x4x1_16b_f32 v[40:43], v32, v32, 0
	v_mfma_f32_4x4x1_16b_f32 v[44:47], v32, v32, 0
	v_mfma_f32_4x4x1_16b_f32 v[48:51], v32, v32, 0
	v_mfma_f32_4x4x1_16b_f32 v[52:55], v32, v32, 0
	v_mfma_f32_4x4x1_16b_f32 v[56:59], v32, v32, 0
	v_mfma_f32_4x4x1_16b_f32 v[60:63], v32, v32, 0
	v_mfma_f32_4x4x1_16b_f32 v[64:67], v32, v32, 0
	v_mfma_f32_4x4x1_16b_f32 v[68:71], v32, v32, 0
	v_mfma_f32_4x4x1_16b_f32 v[72:75], v32, v32, 0
	v_mfma_f32_4x4x1_16b_f32 v[76:79], v32, v32, 0
	v_mfma_f32_4x4x1_16b_f32 v[80:83], v32, v32, 0
	v_mfma_f32_4x4x1_16b_f32 v[84:87], v32, v32, 0
	v_mfma_f32_4x4x1_16b_f32 v[88:91], v32, v32, 0
	v_mfma_f32_4x4x1_16b_f32 v[92:95], v32, v32, 0
	v_mfma_f32_4x4x1_16b_f32 v[96:99], v32, v32, 0
	v_mfma_f32_4x4x1_16b_f32 v[100:103], v32, v32, 0
	v_mfma_f32_4x4x1_16b_f32 v[104:107], v32, v32, 0
	v_mfma_f32_4x4x1_16b_f32 v[108:111], v32, v32, 0
	v_mfma_f32_4x4x1_16b_f32 v[112:115], v32, v32, 0
	v_mfma_f32_4x4x1_16b_f32 v[116:119], v32, v32, 0
	v_mfma_f32_4x4x1_16b_f32 v[120:123], v32, v32, 0
	v_mfma_f32_4x4x1_16b_f32 v[124:127], v32, v32, 0
	v_mfma_f32_4x4x1_16b_f32 v[128:131], v32, v32, 0
	v_mfma_f32_4x4x1_16b_f32 v[132:135], v32, v32, 0
	v_mfma_f32_4x4x1_16b_f32 v[136:139], v32, v32, 0
	v_mfma_f32_4x4x1_16b_f32 v[140:143], v32, v32, 0
	v_mfma_f32_4x4x1_16b_f32 v[144:147], v32, v32, 0
	v_mfma_f32_4x4x1_16b_f32 v[148:151], v32, v32, 0
	v_mfma_f32_4x4x1_16b_f32 v[152:155], v32, v32, 0
	v_mfma_f32_4x4x1_16b_f32 v[156:159], v32, v32, 0
	v_mfma_f32_4x4x1_16b_f32 v[32:35], v32, v32, 0
